# v44 + FOX unit prologue: wave-wide maxima of the QK-norm gains via v_permlane32/16_swap + DPP row_ror instead of 12 ds_bpermute round trips
# baseline (speedup 1.0000x reference)
; template <bool FOX>
; __device__ __forceinline__ void attn_unit(const Args& A, int b, int h, int qb, LAS char* shm, LAS float* dg) {
;     ...
;         float gq = fmaxf(fabsf(A.gfq[lane]), 0.f), gk = fabsf(A.gfk[lane]);
; #pragma unroll
;         for (int o = 32; o > 0; o >>= 1) { gq = fmaxf(gq, __shfl_xor(gq, o)); gk = fmaxf(gk, __shfl_xor(gk, o)); }
;         const float margin = 2.f * (8.f * gq * gk) + SKIP_NATS;
;         const float Fref = A.F[(rowbase + q0) * 8 + h];
;         const int nfull = q0 / 64;
;         bool keep0 = true, keep1 = true;
;         if (lane < nfull) keep0 = (Fref - A.F[(rowbase + 64 * lane + 63) * 8 + h]) >= -margin;
.LBB0_926:
	s_or_b64 exec, exec, s[12:13]
	s_bitcmp0_b32 s3, 0
	s_cselect_b64 s[4:5], -1, 0
	s_cmp_ge_i32 s2, s74
	s_cselect_b64 s[6:7], -1, 0
	s_or_b64 s[4:5], s[4:5], s[6:7]
	s_mov_b64 s[12:13], -1
	s_and_b64 vcc, exec, s[4:5]
	s_cbranch_vccz .LBB0_1017
	v_mov_b32_e32 v128, v0
	v_and_b32_e32 v6, 64, v237
	v_and_b32_e32 v191, 63, v128
	v_lshlrev_b32_e32 v3, 2, v191
	global_load_dword v4, v3, s[36:37]
	v_add_u32_e32 v6, 64, v6
	global_load_dword v3, v3, s[88:89]
	v_xor_b32_e32 v7, 32, v237
	v_cmp_lt_i32_e32 vcc, v7, v6
	s_not_b32 s3, s1
	s_bfe_u32 s3, s3, 0x50002
	v_cndmask_b32_e32 v7, v237, v7, vcc
	v_lshlrev_b32_e32 v7, 2, v7
	s_and_b32 s4, s1, 3
	s_lshl_b32 s6, s4, 13
	s_lshl_b32 s5, s3, 8
	s_or_b32 s8, s5, s6
	s_ashr_i32 s1, s0, 31
	s_lshl_b32 s8, s8, 5
	s_add_u32 s8, s34, s8
	s_addc_u32 s15, s35, 0
	s_lshl_b64 s[12:13], s[0:1], 2
	s_add_u32 s14, s8, s12
	s_addc_u32 s15, s15, s13
	s_lshl_b32 s3, s3, 2
	v_readfirstlane_b32 s7, v128
	s_mov_b64 s[18:19], -1
	s_waitcnt vmcnt(1)
	v_max_f32_e64 v4, |v4|, |v4|
	v_max_f32_e32 v4, 0, v4
	s_waitcnt vmcnt(0)
	v_max_f32_e64 v5, |v3|, |v3|
	v_mov_b32_e32 v7, v4
	v_mov_b32_e32 v8, v5
	s_nop 1
	v_permlane32_swap_b32_e32 v4, v7
	v_permlane32_swap_b32_e32 v5, v8
	v_max_f32_e32 v4, v4, v7
	v_max_f32_e32 v5, v5, v8
	v_mov_b32_e32 v7, v4
	v_mov_b32_e32 v8, v5
	s_nop 1
	v_permlane16_swap_b32_e32 v4, v7
	v_permlane16_swap_b32_e32 v5, v8
	v_max_f32_e32 v4, v4, v7
	v_max_f32_e32 v5, v5, v8
	s_nop 1
	v_max_f32_dpp v4, v4, v4 row_ror:8 row_mask:0xf bank_mask:0xf
	v_max_f32_dpp v5, v5, v5 row_ror:8 row_mask:0xf bank_mask:0xf
	s_nop 1
	v_max_f32_dpp v4, v4, v4 row_ror:4 row_mask:0xf bank_mask:0xf
	v_max_f32_dpp v5, v5, v5 row_ror:4 row_mask:0xf bank_mask:0xf
	s_nop 1
	v_max_f32_dpp v4, v4, v4 row_ror:2 row_mask:0xf bank_mask:0xf
	v_max_f32_dpp v5, v5, v5 row_ror:2 row_mask:0xf bank_mask:0xf
	s_nop 1
	v_max_f32_dpp v4, v4, v4 row_ror:1 row_mask:0xf bank_mask:0xf
	v_max_f32_dpp v5, v5, v5 row_ror:1 row_mask:0xf bank_mask:0xf
	s_nop 1
	v_xor_b32_e32 v3, 4, v237
	v_cmp_lt_i32_e32 vcc, v3, v6
	s_nop 1
	v_cndmask_b32_e32 v3, v237, v3, vcc
	v_lshlrev_b32_e32 v3, 2, v3
	v_xor_b32_e32 v7, 2, v237
	v_cmp_lt_i32_e32 vcc, v7, v6
	s_nop 1
	v_cndmask_b32_e32 v7, v237, v7, vcc
	v_lshlrev_b32_e32 v134, 2, v7
	v_xor_b32_e32 v7, 1, v237
	v_cmp_lt_i32_e32 vcc, v7, v6
	s_nop 1
	v_cndmask_b32_e32 v6, v237, v7, vcc
	v_lshlrev_b32_e32 v190, 2, v6
	v_cmp_gt_u32_e32 vcc, s3, v191
	v_mul_f32_e32 v4, 0x41000000, v4
	v_mul_f32_e32 v4, v5, v4
	v_mul_f32_e32 v240, 0x3fb8aa3b, v4
	v_fmaak_f32 v5, 2.0, v4, 0x42000000
	global_load_dword v4, v131, s[14:15]
	s_mov_b64 s[14:15], -1
	s_and_saveexec_b64 s[22:23], vcc
	s_cbranch_execz .LBB0_929
	s_lshl_b32 s8, s4, 18
	v_lshl_or_b32 v130, v191, 11, s8
	v_lshl_add_u64 v[6:7], s[34:35], 0, v[130:131]
	v_lshl_add_u64 v[6:7], s[0:1], 2, v[6:7]
	global_load_dword v6, v[6:7], off offset:2016
	s_waitcnt vmcnt(0)
	v_sub_f32_e32 v6, v4, v6
	v_cmp_ge_f32_e64 s[18:19], v6, -v5
	s_orn2_b64 s[18:19], s[18:19], exec
